# conversion kernel: first generation of workgroups staggered in 8 steps of ~0.4 us; LDS-DMA gather at 4 workgroups per CU unchanged
# baseline (speedup 1.0000x reference)
_Z10cvt_kernelPKDv4_fPDv4_DF16_:
	s_load_dwordx4 s[4:7], s[0:1], 0x0
	s_and_b32 s3, s2, 7
	s_lshr_b32 s8, s2, 3
	s_cmp_ge_u32 s8, 256
	s_cbranch_scc1 .Lcvt_nostag
	s_bfe_u32 s9, s8, 0x30005
	s_cmp_eq_u32 s9, 0
	s_cbranch_scc1 .Lcvt_nostag
.Lcvt_stag:
	s_sleep 15
	s_sub_u32 s9, s9, 1
	s_cmp_lg_u32 s9, 0
	s_cbranch_scc1 .Lcvt_stag
.Lcvt_nostag:
	s_cmpk_ge_u32 s2, 0x7a10
	s_cbranch_scc1 .Lcvt_left
	s_mulk_i32 s3, 0xf42
	s_add_i32 s0, s3, s8
	s_sub_u32 s9, 0xf42, s8
	s_min_u32 s9, s9, 1
	s_branch .Lcvt_go
